# v8 + P0b: int8 H1 rows (the in-proj GEMM's A operand, consumed by the next phase) stored without nt so they stay in L2/MALL
# speedup vs baseline: 1.0012x; 1.0011x over previous
; #define GAS __attribute__((address_space(1)))
; #define LDS_WAIT() asm volatile("s_waitcnt lgkmcnt(0)" ::: "memory")
; DI unsigned pk2(float lo, float hi) { return f2bf(lo) | (f2bf(hi) << 16); }
; DI float lane_bcast(float v, int l) { return __uint_as_float((unsigned)__builtin_amdgcn_readlane((int)__float_as_uint(v), l)); }
; DI void p0b_phase(Frame& F) {
;     ...
;             v2u o; o.x = pk2(h0.x, h0.y); o.y = pk2(h0.z, h0.w); o8[64 * j] = o; am0 = fmaxf(am0, fmaxf(fmaxf(fabsf(h0.x), fabsf(h0.y)), fmaxf(fabsf(h0.z), fabsf(h0.w))));
;             o.x = pk2(h1.x, h1.y); o.y = pk2(h1.z, h1.w); o8[512 + 64 * j] = o; am1 = fmaxf(am1, fmaxf(fmaxf(fabsf(h1.x), fabsf(h1.y)), fmaxf(fabsf(h1.z), fabsf(h1.w))));
;     ...
;             const float amt = red2_max(am0, am1);
;             LDS_WAIT(); asm volatile("" ::: "memory");
; #pragma unroll
;             for (int r = 0; r < 2; ++r) {
;                 const float am = fmaxf(lane_bcast(amt, 32 * r), 1e-30f), qinv = 127.0f / am;
;                 GAS unsigned* qr = (GAS unsigned*)(F.H1Q + (size_t)(row + r) * D) + F.lane;
; #pragma unroll
;                 for (int j = 0; j < 8; ++j) { const v2u w = o8[512 * r + 64 * j];
;                     const int q0 = (int)__builtin_rintf(bflo(w.x) * qinv), q1 = (int)__builtin_rintf(bfhi(w.x) * qinv), q2 = (int)__builtin_rintf(bflo(w.y) * qinv), q3 = (int)__builtin_rintf(bfhi(w.y) * qinv);
;                     __builtin_nontemporal_store((unsigned)(q0 & 255) | ((unsigned)(q1 & 255) << 8) | ((unsigned)(q2 & 255) << 16) | ((unsigned)(q3 & 255) << 24), qr + 64 * j); }
;                 if (F.lane == 0) F.SA[row + r] = am * (1.0f / 127.0f);
.LBB0_204:
	s_or_b64 exec, exec, s[14:15]
	v_max_f32_e64 v129, |v129|, |v129|
	v_max_f32_e64 v128, |v128|, |v128|
	v_max_f32_e64 v125, |v125|, |v125|
	v_max_f32_e64 v124, |v124|, |v124|
	v_max_f32_e64 v121, |v121|, |v121|
	v_max_f32_e64 v120, |v120|, |v120|
	v_max_f32_e64 v117, |v117|, |v117|
	v_max_f32_e64 v116, |v116|, |v116|
	v_max_f32_e32 v128, v128, v129
	v_max_f32_e32 v124, v124, v125
	v_max_f32_e32 v120, v120, v121
	v_max_f32_e32 v116, v116, v117
	v_max_f32_e64 v113, |v113|, |v113|
	v_max_f32_e64 v112, |v112|, |v112|
	v_max_f32_e64 v109, |v109|, |v109|
	v_max_f32_e64 v108, |v108|, |v108|
	v_max_f32_e64 v105, |v105|, |v105|
	v_max_f32_e64 v104, |v104|, |v104|
	v_max_f32_e64 v101, |v101|, |v101|
	v_max_f32_e64 v100, |v100|, |v100|
	v_max3_f32 v126, |v126|, |v127|, v128
	v_max3_f32 v122, |v122|, |v123|, v124
	v_max3_f32 v118, |v118|, |v119|, v120
	v_max3_f32 v114, |v114|, |v115|, v116
	v_max_f32_e32 v112, v112, v113
	v_max_f32_e32 v108, v108, v109
	v_max_f32_e32 v104, v104, v105
	v_max_f32_e32 v100, v100, v101
	v_max_f32_e64 v97, |v97|, |v97|
	v_max_f32_e64 v96, |v96|, |v96|
	v_max_f32_e64 v93, |v93|, |v93|
	v_max_f32_e64 v92, |v92|, |v92|
	v_max_f32_e64 v89, |v89|, |v89|
	v_max_f32_e64 v88, |v88|, |v88|
	v_max_f32_e64 v85, |v85|, |v85|
	v_max_f32_e64 v84, |v84|, |v84|
	v_max3_f32 v115, v126, 0, v118
	v_max3_f32 v114, v122, 0, v114
	v_max3_f32 v110, |v110|, |v111|, v112
	v_max3_f32 v106, |v106|, |v107|, v108
	v_max3_f32 v102, |v102|, |v103|, v104
	v_max3_f32 v98, |v98|, |v99|, v100
	v_max_f32_e32 v96, v96, v97
	v_max_f32_e32 v92, v92, v93
	v_max_f32_e32 v88, v88, v89
	v_max_f32_e32 v84, v84, v85
	v_max_f32_e64 v81, |v81|, |v81|
	v_max_f32_e64 v80, |v80|, |v80|
	v_max_f32_e64 v77, |v77|, |v77|
	v_max_f32_e64 v76, |v76|, |v76|
	v_max_f32_e64 v73, |v73|, |v73|
	v_max_f32_e64 v72, |v72|, |v72|
	v_max_f32_e64 v69, |v69|, |v69|
	v_max_f32_e64 v68, |v68|, |v68|
	v_max3_f32 v99, v115, v110, v102
	v_max3_f32 v98, v114, v106, v98
	v_max3_f32 v94, |v94|, |v95|, v96
	v_max3_f32 v90, |v90|, |v91|, v92
	v_max3_f32 v86, |v86|, |v87|, v88
	v_max3_f32 v82, |v82|, |v83|, v84
	v_max_f32_e32 v80, v80, v81
	v_max_f32_e32 v76, v76, v77
	v_max_f32_e32 v72, v72, v73
	v_max_f32_e32 v68, v68, v69
	v_max3_f32 v83, v99, v94, v86
	v_max3_f32 v82, v98, v90, v82
	v_max3_f32 v78, |v78|, |v79|, v80
	v_max3_f32 v74, |v74|, |v75|, v76
	v_max3_f32 v70, |v70|, |v71|, v72
	v_max3_f32 v66, |v66|, |v67|, v68
	v_max3_f32 v67, v83, v78, v70
	v_max3_f32 v66, v82, v74, v66
	s_nop 1
	v_permlane32_swap_b32_e32 v67, v66
	v_max_f32_e32 v66, v66, v66
	v_max_f32_e32 v67, v67, v67
	v_max_f32_e32 v66, v67, v66
	v_mov_b32_e32 v67, v66
	s_nop 1
	v_permlane16_swap_b32_e32 v66, v67
	v_max_f32_e32 v67, v67, v67
	v_max_f32_e32 v66, v66, v66
	v_max_f32_e32 v66, v66, v67
	s_waitcnt lgkmcnt(0)
	s_nop 1
	v_mov_b32_dpp v67, v66 row_ror:8 row_mask:0xf bank_mask:0xf bound_ctrl:1
	v_max_f32_e32 v67, v67, v67
	v_max_f32_e32 v66, v66, v67
	s_nop 1
	v_mov_b32_dpp v67, v66 row_half_mirror row_mask:0xf bank_mask:0xf bound_ctrl:1
	v_max_f32_e32 v67, v67, v67
	v_max_f32_e32 v66, v66, v67
	s_nop 1
	v_mov_b32_dpp v67, v66 quad_perm:[1,0,3,2] row_mask:0xf bank_mask:0xf bound_ctrl:1
	v_max_f32_e32 v67, v67, v67
	v_max_f32_e32 v66, v66, v67
	s_nop 1
	v_mov_b32_dpp v67, v66 quad_perm:[2,3,0,1] row_mask:0xf bank_mask:0xf bound_ctrl:1
	v_max_f32_e32 v67, v67, v67
	v_max_f32_e32 v68, v66, v67
	s_nop 0
	v_readlane_b32 s14, v68, 0
	s_nop 1
	v_max_f32_e64 v66, s14, s14
	v_max_f32_e32 v69, 0xda24260, v66
	v_div_scale_f32 v66, s[14:15], v69, v69, s42
	v_rcp_f32_e32 v67, v66
	s_brev_b32 s14, 40
	v_fma_f32 v70, -v66, v67, 1.0
	v_fmac_f32_e32 v67, v70, v67
	v_div_scale_f32 v70, vcc, s42, v69, s42
	v_mul_f32_e32 v74, v70, v67
	v_fma_f32 v71, -v66, v74, v70
	v_fmac_f32_e32 v74, v71, v67
	v_fma_f32 v66, -v66, v74, v70
	ds_read2st64_b64 v[70:73], v143 offset1:1
	v_div_fmas_f32 v66, v66, v67, v74
	v_div_fixup_f32 v78, v66, v69, s42
	ds_read2st64_b64 v[74:77], v143 offset0:2 offset1:3
	v_lshl_add_u64 v[66:67], s[48:49], 0, v[134:135]
	s_waitcnt lgkmcnt(1)
	v_lshlrev_b32_e32 v79, 16, v70
	v_and_b32_e32 v70, 0xffff0000, v70
	v_mul_f32_e32 v70, v78, v70
	v_lshlrev_b32_e32 v80, 16, v71
	v_and_b32_e32 v71, 0xffff0000, v71
	v_mul_f32_e32 v79, v78, v79
	v_rndne_f32_e32 v70, v70
	v_mul_f32_e32 v80, v78, v80
	v_mul_f32_e32 v71, v78, v71
	v_rndne_f32_e32 v79, v79
	v_cvt_i32_f32_e32 v70, v70
	v_rndne_f32_e32 v80, v80
	v_rndne_f32_e32 v71, v71
	v_cvt_i32_f32_e32 v79, v79
	v_cvt_i32_f32_sdwa v80, v80 dst_sel:WORD_1 dst_unused:UNUSED_PAD src0_sel:DWORD
	v_cvt_i32_f32_e32 v71, v71
	v_lshlrev_b32_e32 v70, 8, v70
	v_and_b32_e32 v70, 0xff00, v70
	v_and_b32_e32 v80, 0xff0000, v80
	v_perm_b32 v71, v71, v79, s43
	v_add_co_u32_e32 v66, vcc, s14, v66
	v_or3_b32 v70, v71, v70, v80
	s_nop 0
	v_addc_co_u32_e32 v67, vcc, 0, v67, vcc
	v_and_b32_e32 v71, 0xffff0000, v72
	global_store_dword v[66:67], v70, off
	v_lshlrev_b32_e32 v70, 16, v72
	v_mul_f32_e32 v71, v78, v71
	v_lshlrev_b32_e32 v72, 16, v73
	v_and_b32_e32 v73, 0xffff0000, v73
	v_mul_f32_e32 v70, v78, v70
	v_rndne_f32_e32 v71, v71
	v_mul_f32_e32 v72, v78, v72
	v_mul_f32_e32 v73, v78, v73
	v_rndne_f32_e32 v70, v70
	v_cvt_i32_f32_e32 v71, v71
	v_rndne_f32_e32 v72, v72
	v_rndne_f32_e32 v73, v73
	v_cvt_i32_f32_e32 v70, v70
	v_cvt_i32_f32_sdwa v72, v72 dst_sel:WORD_1 dst_unused:UNUSED_PAD src0_sel:DWORD
	v_cvt_i32_f32_e32 v73, v73
	v_lshlrev_b32_e32 v71, 8, v71
	v_and_b32_e32 v71, 0xff00, v71
	v_and_b32_e32 v72, 0xff0000, v72
	v_perm_b32 v70, v73, v70, s43
	v_or3_b32 v70, v70, v71, v72
	s_waitcnt lgkmcnt(0)
; #define GAS __attribute__((address_space(1)))
; DI float lane_bcast(float v, int l) { return __uint_as_float((unsigned)__builtin_amdgcn_readlane((int)__float_as_uint(v), l)); }
; DI void p0b_phase(Frame& F) {
;     ...
;             for (int r = 0; r < 2; ++r) {
;                 const float am = fmaxf(lane_bcast(amt, 32 * r), 1e-30f), qinv = 127.0f / am;
;                 GAS unsigned* qr = (GAS unsigned*)(F.H1Q + (size_t)(row + r) * D) + F.lane;
; #pragma unroll
;                 for (int j = 0; j < 8; ++j) { const v2u w = o8[512 * r + 64 * j];
;                     const int q0 = (int)__builtin_rintf(bflo(w.x) * qinv), q1 = (int)__builtin_rintf(bfhi(w.x) * qinv), q2 = (int)__builtin_rintf(bflo(w.y) * qinv), q3 = (int)__builtin_rintf(bfhi(w.y) * qinv);
;                     __builtin_nontemporal_store((unsigned)(q0 & 255) | ((unsigned)(q1 & 255) << 8) | ((unsigned)(q2 & 255) << 16) | ((unsigned)(q3 & 255) << 24), qr + 64 * j); }
;                 if (F.lane == 0) F.SA[row + r] = am * (1.0f / 127.0f);
	v_and_b32_e32 v71, 0xffff0000, v74
	global_store_dword v[66:67], v70, off offset:256
	v_lshlrev_b32_e32 v70, 16, v74
	v_mul_f32_e32 v71, v78, v71
	v_lshlrev_b32_e32 v72, 16, v75
	v_and_b32_e32 v73, 0xffff0000, v75
	v_mul_f32_e32 v70, v78, v70
	v_rndne_f32_e32 v71, v71
	v_mul_f32_e32 v72, v78, v72
	v_mul_f32_e32 v73, v78, v73
	v_rndne_f32_e32 v70, v70
	v_cvt_i32_f32_e32 v71, v71
	v_rndne_f32_e32 v72, v72
	v_rndne_f32_e32 v73, v73
	v_cvt_i32_f32_e32 v70, v70
	v_cvt_i32_f32_sdwa v72, v72 dst_sel:WORD_1 dst_unused:UNUSED_PAD src0_sel:DWORD
	v_cvt_i32_f32_e32 v73, v73
	v_lshlrev_b32_e32 v71, 8, v71
	v_and_b32_e32 v71, 0xff00, v71
	v_and_b32_e32 v72, 0xff0000, v72
	v_perm_b32 v70, v73, v70, s43
	v_or3_b32 v70, v70, v71, v72
	global_store_dword v[66:67], v70, off offset:512
	v_lshlrev_b32_e32 v70, 16, v76
	v_mul_f32_e32 v70, v78, v70
	v_rndne_f32_e32 v70, v70
	v_cvt_i32_f32_e32 v74, v70
	v_and_b32_e32 v70, 0xffff0000, v76
	v_mul_f32_e32 v70, v78, v70
	v_lshlrev_b32_e32 v71, 16, v77
	v_rndne_f32_e32 v70, v70
	v_mul_f32_e32 v71, v78, v71
	v_cvt_i32_f32_e32 v70, v70
	v_rndne_f32_e32 v71, v71
	v_cvt_i32_f32_sdwa v71, v71 dst_sel:WORD_1 dst_unused:UNUSED_PAD src0_sel:DWORD
	v_and_b32_e32 v72, 0xffff0000, v77
	v_mul_f32_e32 v72, v78, v72
	v_rndne_f32_e32 v72, v72
	v_cvt_i32_f32_e32 v75, v72
	v_lshlrev_b32_e32 v70, 8, v70
	v_and_b32_e32 v76, 0xff00, v70
	v_and_b32_e32 v77, 0xff0000, v71
	ds_read2st64_b64 v[70:73], v143 offset0:4 offset1:5
	v_perm_b32 v74, v75, v74, s43
	v_or3_b32 v74, v74, v76, v77
	global_store_dword v[66:67], v74, off offset:768
	ds_read2st64_b64 v[74:77], v143 offset0:6 offset1:7
	s_waitcnt lgkmcnt(1)
	v_lshlrev_b32_e32 v79, 16, v70
	v_and_b32_e32 v70, 0xffff0000, v70
	v_mul_f32_e32 v70, v78, v70
	v_lshlrev_b32_e32 v80, 16, v71
	v_and_b32_e32 v71, 0xffff0000, v71
	v_mul_f32_e32 v79, v78, v79
	v_rndne_f32_e32 v70, v70
	v_mul_f32_e32 v80, v78, v80
	v_mul_f32_e32 v71, v78, v71
	v_rndne_f32_e32 v79, v79
	v_cvt_i32_f32_e32 v70, v70
	v_rndne_f32_e32 v80, v80
	v_rndne_f32_e32 v71, v71
	v_cvt_i32_f32_e32 v79, v79
	v_cvt_i32_f32_sdwa v80, v80 dst_sel:WORD_1 dst_unused:UNUSED_PAD src0_sel:DWORD
	v_cvt_i32_f32_e32 v71, v71
	v_lshlrev_b32_e32 v70, 8, v70
	v_and_b32_e32 v70, 0xff00, v70
	v_and_b32_e32 v80, 0xff0000, v80
	v_perm_b32 v71, v71, v79, s43
	v_or3_b32 v70, v71, v70, v80
	v_and_b32_e32 v71, 0xffff0000, v72
	global_store_dword v[66:67], v70, off offset:1024
	v_lshlrev_b32_e32 v70, 16, v72
	v_mul_f32_e32 v71, v78, v71
	v_lshlrev_b32_e32 v72, 16, v73
	v_and_b32_e32 v73, 0xffff0000, v73
	v_mul_f32_e32 v70, v78, v70
	v_rndne_f32_e32 v71, v71
	v_mul_f32_e32 v72, v78, v72
	v_mul_f32_e32 v73, v78, v73
	v_rndne_f32_e32 v70, v70
	v_cvt_i32_f32_e32 v71, v71
	v_rndne_f32_e32 v72, v72
	v_rndne_f32_e32 v73, v73
	v_cvt_i32_f32_e32 v70, v70
	v_cvt_i32_f32_sdwa v72, v72 dst_sel:WORD_1 dst_unused:UNUSED_PAD src0_sel:DWORD
	v_cvt_i32_f32_e32 v73, v73
	v_lshlrev_b32_e32 v71, 8, v71
	v_and_b32_e32 v71, 0xff00, v71
	v_and_b32_e32 v72, 0xff0000, v72
	v_perm_b32 v70, v73, v70, s43
	v_or3_b32 v70, v70, v71, v72
	s_waitcnt lgkmcnt(0)
	v_and_b32_e32 v71, 0xffff0000, v74
	global_store_dword v[66:67], v70, off offset:1280
	v_lshlrev_b32_e32 v70, 16, v74
	v_mul_f32_e32 v71, v78, v71
	v_lshlrev_b32_e32 v72, 16, v75
	v_and_b32_e32 v73, 0xffff0000, v75
	v_mul_f32_e32 v70, v78, v70
	v_rndne_f32_e32 v71, v71
	v_mul_f32_e32 v72, v78, v72
	v_mul_f32_e32 v73, v78, v73
	v_rndne_f32_e32 v70, v70
	v_cvt_i32_f32_e32 v71, v71
	v_rndne_f32_e32 v72, v72
	v_rndne_f32_e32 v73, v73
	v_cvt_i32_f32_e32 v70, v70
	v_cvt_i32_f32_sdwa v72, v72 dst_sel:WORD_1 dst_unused:UNUSED_PAD src0_sel:DWORD
	v_cvt_i32_f32_e32 v73, v73
	v_lshlrev_b32_e32 v71, 8, v71
	v_and_b32_e32 v71, 0xff00, v71
	v_and_b32_e32 v72, 0xff0000, v72
	v_perm_b32 v70, v73, v70, s43
	v_or3_b32 v70, v70, v71, v72
	v_and_b32_e32 v71, 0xffff0000, v76
	global_store_dword v[66:67], v70, off offset:1536
	v_lshlrev_b32_e32 v70, 16, v76
	v_mul_f32_e32 v71, v78, v71
	v_lshlrev_b32_e32 v72, 16, v77
	v_and_b32_e32 v73, 0xffff0000, v77
	v_mul_f32_e32 v70, v78, v70
	v_rndne_f32_e32 v71, v71
	v_mul_f32_e32 v72, v78, v72
	v_mul_f32_e32 v73, v78, v73
	v_rndne_f32_e32 v70, v70
	v_cvt_i32_f32_e32 v71, v71
	v_rndne_f32_e32 v72, v72
	v_rndne_f32_e32 v73, v73
	v_cvt_i32_f32_e32 v70, v70
	v_cvt_i32_f32_sdwa v72, v72 dst_sel:WORD_1 dst_unused:UNUSED_PAD src0_sel:DWORD
	v_cvt_i32_f32_e32 v73, v73
	v_lshlrev_b32_e32 v71, 8, v71
	v_and_b32_e32 v71, 0xff00, v71
	v_and_b32_e32 v72, 0xff0000, v72
	v_perm_b32 v70, v73, v70, s43
	v_or3_b32 v70, v70, v71, v72
	global_store_dword v[66:67], v70, off offset:1792
	s_and_saveexec_b64 s[14:15], s[6:7]
	s_cbranch_execz .LBB0_206
	s_add_u32 s34, s48, s22
	s_addc_u32 s35, s49, s23
	v_mul_f32_e32 v69, 0x3c010204, v69
	global_store_dword v158, v69, s[34:35]
; #define GAS __attribute__((address_space(1)))
; DI float lane_bcast(float v, int l) { return __uint_as_float((unsigned)__builtin_amdgcn_readlane((int)__float_as_uint(v), l)); }
; DI void p0b_phase(Frame& F) {
;     ...
;             for (int r = 0; r < 2; ++r) {
;                 const float am = fmaxf(lane_bcast(amt, 32 * r), 1e-30f), qinv = 127.0f / am;
;                 GAS unsigned* qr = (GAS unsigned*)(F.H1Q + (size_t)(row + r) * D) + F.lane;
; #pragma unroll
;                 for (int j = 0; j < 8; ++j) { const v2u w = o8[512 * r + 64 * j];
;                     const int q0 = (int)__builtin_rintf(bflo(w.x) * qinv), q1 = (int)__builtin_rintf(bfhi(w.x) * qinv), q2 = (int)__builtin_rintf(bflo(w.y) * qinv), q3 = (int)__builtin_rintf(bfhi(w.y) * qinv);
;                     __builtin_nontemporal_store((unsigned)(q0 & 255) | ((unsigned)(q1 & 255) << 8) | ((unsigned)(q2 & 255) << 16) | ((unsigned)(q3 & 255) << 24), qr + 64 * j); }
;                 if (F.lane == 0) F.SA[row + r] = am * (1.0f / 127.0f);
.LBB0_206:
	s_or_b64 exec, exec, s[14:15]
	v_readlane_b32 s14, v68, 32
	s_nop 1
	v_max_f32_e64 v68, s14, s14
	v_max_f32_e32 v68, 0xda24260, v68
	v_div_scale_f32 v69, s[14:15], v68, v68, s42
	v_rcp_f32_e32 v74, v69
	v_div_scale_f32 v70, vcc, s42, v68, s42
	v_fma_f32 v71, -v69, v74, 1.0
	v_fmac_f32_e32 v74, v71, v74
	v_mul_f32_e32 v75, v70, v74
	v_fma_f32 v71, -v69, v75, v70
	v_fmac_f32_e32 v75, v71, v74
	v_fma_f32 v69, -v69, v75, v70
	ds_read2st64_b64 v[70:73], v143 offset0:8 offset1:9
	v_div_fmas_f32 v69, v69, v74, v75
	v_div_fixup_f32 v69, v69, v68, s42
	ds_read2st64_b64 v[74:77], v143 offset0:10 offset1:11
	s_waitcnt lgkmcnt(1)
	v_lshlrev_b32_e32 v78, 16, v70
	v_and_b32_e32 v70, 0xffff0000, v70
	v_mul_f32_e32 v70, v69, v70
	v_lshlrev_b32_e32 v79, 16, v71
	v_and_b32_e32 v71, 0xffff0000, v71
	v_mul_f32_e32 v78, v69, v78
	v_rndne_f32_e32 v70, v70
	v_mul_f32_e32 v79, v69, v79
	v_mul_f32_e32 v71, v69, v71
	v_rndne_f32_e32 v78, v78
	v_cvt_i32_f32_e32 v70, v70
	v_rndne_f32_e32 v79, v79
	v_rndne_f32_e32 v71, v71
	v_cvt_i32_f32_e32 v78, v78
	v_cvt_i32_f32_sdwa v79, v79 dst_sel:WORD_1 dst_unused:UNUSED_PAD src0_sel:DWORD
	v_cvt_i32_f32_e32 v71, v71
	v_lshlrev_b32_e32 v70, 8, v70
	v_and_b32_e32 v70, 0xff00, v70
	v_and_b32_e32 v79, 0xff0000, v79
	v_perm_b32 v71, v71, v78, s43
	v_or3_b32 v70, v71, v70, v79
	v_and_b32_e32 v71, 0xffff0000, v72
	global_store_dword v[66:67], v70, off offset:2048
	v_lshlrev_b32_e32 v70, 16, v72
	v_mul_f32_e32 v71, v69, v71
	v_lshlrev_b32_e32 v72, 16, v73
	v_and_b32_e32 v73, 0xffff0000, v73
	v_mul_f32_e32 v70, v69, v70
	v_rndne_f32_e32 v71, v71
	v_mul_f32_e32 v72, v69, v72
	v_mul_f32_e32 v73, v69, v73
	v_rndne_f32_e32 v70, v70
	v_cvt_i32_f32_e32 v71, v71
	v_rndne_f32_e32 v72, v72
	v_rndne_f32_e32 v73, v73
	v_cvt_i32_f32_e32 v70, v70
	v_cvt_i32_f32_sdwa v72, v72 dst_sel:WORD_1 dst_unused:UNUSED_PAD src0_sel:DWORD
	v_cvt_i32_f32_e32 v73, v73
	v_lshlrev_b32_e32 v71, 8, v71
	v_and_b32_e32 v71, 0xff00, v71
	v_and_b32_e32 v72, 0xff0000, v72
	v_perm_b32 v70, v73, v70, s43
	v_or3_b32 v70, v70, v71, v72
	s_waitcnt lgkmcnt(0)
	v_and_b32_e32 v71, 0xffff0000, v74
	global_store_dword v[66:67], v70, off offset:2304
	v_lshlrev_b32_e32 v70, 16, v74
	v_mul_f32_e32 v71, v69, v71
	v_lshlrev_b32_e32 v72, 16, v75
	v_and_b32_e32 v73, 0xffff0000, v75
	v_mul_f32_e32 v70, v69, v70
	v_rndne_f32_e32 v71, v71
	v_mul_f32_e32 v72, v69, v72
	v_mul_f32_e32 v73, v69, v73
	v_rndne_f32_e32 v70, v70
	v_cvt_i32_f32_e32 v71, v71
	v_rndne_f32_e32 v72, v72
	v_rndne_f32_e32 v73, v73
	v_cvt_i32_f32_e32 v70, v70
	v_cvt_i32_f32_sdwa v72, v72 dst_sel:WORD_1 dst_unused:UNUSED_PAD src0_sel:DWORD
	v_cvt_i32_f32_e32 v73, v73
	v_lshlrev_b32_e32 v71, 8, v71
	v_and_b32_e32 v71, 0xff00, v71
	v_and_b32_e32 v72, 0xff0000, v72
	v_perm_b32 v70, v73, v70, s43
	v_or3_b32 v70, v70, v71, v72
	global_store_dword v[66:67], v70, off offset:2560
	v_lshlrev_b32_e32 v70, 16, v76
	v_mul_f32_e32 v70, v69, v70
	v_rndne_f32_e32 v70, v70
	v_cvt_i32_f32_e32 v74, v70
	v_and_b32_e32 v70, 0xffff0000, v76
	v_mul_f32_e32 v70, v69, v70
	v_lshlrev_b32_e32 v71, 16, v77
	v_rndne_f32_e32 v70, v70
	v_mul_f32_e32 v71, v69, v71
	v_cvt_i32_f32_e32 v70, v70
	v_rndne_f32_e32 v71, v71
	v_cvt_i32_f32_sdwa v71, v71 dst_sel:WORD_1 dst_unused:UNUSED_PAD src0_sel:DWORD
	v_and_b32_e32 v72, 0xffff0000, v77
	v_mul_f32_e32 v72, v69, v72
	v_rndne_f32_e32 v72, v72
	v_cvt_i32_f32_e32 v75, v72
	v_lshlrev_b32_e32 v70, 8, v70
	v_and_b32_e32 v76, 0xff00, v70
	v_and_b32_e32 v77, 0xff0000, v71
	ds_read2st64_b64 v[70:73], v143 offset0:12 offset1:13
	v_perm_b32 v74, v75, v74, s43
	v_or3_b32 v74, v74, v76, v77
	global_store_dword v[66:67], v74, off offset:2816
	ds_read2st64_b64 v[74:77], v143 offset0:14 offset1:15
	s_waitcnt lgkmcnt(1)
	v_lshlrev_b32_e32 v78, 16, v70
	v_and_b32_e32 v70, 0xffff0000, v70
	v_mul_f32_e32 v70, v69, v70
	v_lshlrev_b32_e32 v79, 16, v71
	v_and_b32_e32 v71, 0xffff0000, v71
	v_mul_f32_e32 v78, v69, v78
	v_rndne_f32_e32 v70, v70
	v_mul_f32_e32 v79, v69, v79
	v_mul_f32_e32 v71, v69, v71
	v_rndne_f32_e32 v78, v78
	v_cvt_i32_f32_e32 v70, v70
	v_rndne_f32_e32 v79, v79
	v_rndne_f32_e32 v71, v71
	v_cvt_i32_f32_e32 v78, v78
	v_cvt_i32_f32_sdwa v79, v79 dst_sel:WORD_1 dst_unused:UNUSED_PAD src0_sel:DWORD
	v_cvt_i32_f32_e32 v71, v71
	v_lshlrev_b32_e32 v70, 8, v70
	v_and_b32_e32 v70, 0xff00, v70
	v_and_b32_e32 v79, 0xff0000, v79
	v_perm_b32 v71, v71, v78, s43
	v_or3_b32 v70, v71, v70, v79
	v_and_b32_e32 v71, 0xffff0000, v72
	global_store_dword v[66:67], v70, off offset:3072
	v_lshlrev_b32_e32 v70, 16, v72
	v_mul_f32_e32 v71, v69, v71
	v_lshlrev_b32_e32 v72, 16, v73
	v_and_b32_e32 v73, 0xffff0000, v73
	v_mul_f32_e32 v70, v69, v70
	v_rndne_f32_e32 v71, v71
	v_mul_f32_e32 v72, v69, v72
	v_mul_f32_e32 v73, v69, v73
	v_rndne_f32_e32 v70, v70
	v_cvt_i32_f32_e32 v71, v71
	v_rndne_f32_e32 v72, v72
	v_rndne_f32_e32 v73, v73
	v_cvt_i32_f32_e32 v70, v70
	v_cvt_i32_f32_sdwa v72, v72 dst_sel:WORD_1 dst_unused:UNUSED_PAD src0_sel:DWORD
	v_cvt_i32_f32_e32 v73, v73
	v_lshlrev_b32_e32 v71, 8, v71
	v_and_b32_e32 v71, 0xff00, v71
	v_and_b32_e32 v72, 0xff0000, v72
	v_perm_b32 v70, v73, v70, s43
	v_or3_b32 v70, v70, v71, v72
	s_waitcnt lgkmcnt(0)
	v_and_b32_e32 v71, 0xffff0000, v74
	global_store_dword v[66:67], v70, off offset:3328
	v_lshlrev_b32_e32 v70, 16, v74
	v_mul_f32_e32 v71, v69, v71
	v_lshlrev_b32_e32 v72, 16, v75
	v_and_b32_e32 v73, 0xffff0000, v75
	v_mul_f32_e32 v70, v69, v70
	v_rndne_f32_e32 v71, v71
	v_mul_f32_e32 v72, v69, v72
	v_mul_f32_e32 v73, v69, v73
	v_rndne_f32_e32 v70, v70
	v_cvt_i32_f32_e32 v71, v71
	v_rndne_f32_e32 v72, v72
	v_rndne_f32_e32 v73, v73
	v_cvt_i32_f32_e32 v70, v70
	v_cvt_i32_f32_sdwa v72, v72 dst_sel:WORD_1 dst_unused:UNUSED_PAD src0_sel:DWORD
	v_cvt_i32_f32_e32 v73, v73
	v_lshlrev_b32_e32 v71, 8, v71
	v_and_b32_e32 v71, 0xff00, v71
	v_and_b32_e32 v72, 0xff0000, v72
	v_perm_b32 v70, v73, v70, s43
	v_or3_b32 v70, v70, v71, v72
	v_and_b32_e32 v71, 0xffff0000, v76
	global_store_dword v[66:67], v70, off offset:3584
	v_lshlrev_b32_e32 v70, 16, v76
	v_mul_f32_e32 v71, v69, v71
	v_lshlrev_b32_e32 v72, 16, v77
	v_and_b32_e32 v73, 0xffff0000, v77
	v_mul_f32_e32 v70, v69, v70
	v_rndne_f32_e32 v71, v71
	v_mul_f32_e32 v72, v69, v72
	v_mul_f32_e32 v69, v69, v73
	v_rndne_f32_e32 v70, v70
	v_cvt_i32_f32_e32 v71, v71
	v_rndne_f32_e32 v72, v72
	v_rndne_f32_e32 v69, v69
	v_cvt_i32_f32_e32 v70, v70
	v_cvt_i32_f32_sdwa v72, v72 dst_sel:WORD_1 dst_unused:UNUSED_PAD src0_sel:DWORD
	v_cvt_i32_f32_e32 v69, v69
	v_lshlrev_b32_e32 v71, 8, v71
	v_and_b32_e32 v71, 0xff00, v71
	v_and_b32_e32 v72, 0xff0000, v72
	v_perm_b32 v69, v69, v70, s43
	v_or3_b32 v69, v69, v71, v72
	global_store_dword v[66:67], v69, off offset:3840
	s_and_saveexec_b64 s[14:15], s[6:7]
	s_cbranch_execz .LBB0_195
	s_add_u32 s34, s48, s22
	s_addc_u32 s35, s49, s23
	v_mul_f32_e32 v66, 0x3c010204, v68
	global_store_dword v158, v66, s[34:35] offset:4
	s_branch .LBB0_195
